# v057 with the carry add of the MLA K tile pointer directly behind its low add (an m0 add between them overwrote SCC)
# speedup vs baseline: 1.0091x; 1.0068x over previous
.LBB0_606:
	s_mul_i32 s46, s26, 0x6000
	s_addk_i32 s46, 0xa000
	s_cmp_lg_u32 s26, 0
	s_cselect_b32 s46, s46, 0xc000
	s_add_i32 s47, s26, 1
	s_cmp_lg_u32 s26, 2
	s_cselect_b32 s26, s47, 0
	s_lshl_b32 s93, s26, 14
	s_add_i32 s47, s76, s93
	s_cmp_eq_u32 s44, 0xbd0000
	s_cbranch_scc1 .LBB0_608
	s_add_i32 m0, s46, s73
	s_add_u32 s98, s52, s44
	s_addc_u32 s99, s53, s45
	global_load_lds_dwordx4 v178, s[98:99]
	s_add_i32 m0, s46, s74
	s_nop 0
	global_load_lds_dwordx4 v180, s[98:99]
	s_add_i32 m0, s46, s75
	s_nop 0
	global_load_lds_dwordx4 v182, s[98:99]
